# speedup vs baseline: 1.0013x; 1.0013x over previous
.Lcsr_cnt_done:
	s_waitcnt lgkmcnt(0)
	s_barrier
	v_mov_b32_e32 v5, 0
	s_and_saveexec_b64 s[20:21], s[6:7]
	ds_read_b32 v5, v3 offset:37168
	s_or_b64 exec, exec, s[20:21]
	s_waitcnt lgkmcnt(0)
	v_mov_b32_e32 v6, v5
	s_nop 4
	v_add_u32_dpp v6, v6, v6 row_shr:1 row_mask:0xf bank_mask:0xf bound_ctrl:0
	s_nop 1
	v_add_u32_dpp v6, v6, v6 row_shr:2 row_mask:0xf bank_mask:0xf bound_ctrl:0
	s_nop 1
	v_add_u32_dpp v6, v6, v6 row_shr:4 row_mask:0xf bank_mask:0xf bound_ctrl:0
	s_nop 1
	v_add_u32_dpp v6, v6, v6 row_shr:8 row_mask:0xf bank_mask:0xf bound_ctrl:0
	s_nop 1
	v_add_u32_dpp v6, v6, v6 row_bcast:15 row_mask:0xa bank_mask:0xf
	s_nop 1
	v_add_u32_dpp v6, v6, v6 row_bcast:31 row_mask:0xc bank_mask:0xf
	s_nop 1
	s_and_saveexec_b64 s[20:21], s[16:17]
	v_lshlrev_b32_e32 v7, 2, v1
	ds_write_b32 v7, v6 offset:38720
	s_or_b64 exec, exec, s[20:21]
	s_waitcnt lgkmcnt(0)
	s_barrier
	s_and_saveexec_b64 s[20:21], s[6:7]
	ds_read_b32 v7, v27 offset:38720
	v_cmp_eq_u32_e64 s[22:23], 1, v1
	v_sub_u32_e32 v6, v6, v5
	s_waitcnt lgkmcnt(0)
	v_cndmask_b32_e64 v7, 0, v7, s[22:23]
	v_add_u32_e32 v6, v6, v7
	ds_write_b32 v3, v6 offset:36640
	s_or_b64 exec, exec, s[20:21]
	s_and_saveexec_b64 s[20:21], s[0:1]
	ds_write_b32 v27, v26 offset:37152
	s_or_b64 exec, exec, s[20:21]
	s_waitcnt lgkmcnt(0)
	s_barrier
	s_cmpk_lt_i32 s33, 0x1
	s_cbranch_scc1 .Lcsr_sc_done
	v_cmp_lt_i32_e64 s[20:21], -1, v28
	v_bfe_u32 v4, v28, 16, 7
	v_lshlrev_b32_e32 v4, 2, v4
	v_cmp_lt_i32_e64 s[22:23], -1, v30
	v_bfe_u32 v5, v30, 16, 7
	v_lshlrev_b32_e32 v5, 2, v5
	v_cmp_lt_i32_e64 s[24:25], -1, v32
	v_bfe_u32 v6, v32, 16, 7
	v_lshlrev_b32_e32 v6, 2, v6
	v_cmp_lt_i32_e64 s[26:27], -1, v34
	v_bfe_u32 v7, v34, 16, 7
	v_lshlrev_b32_e32 v7, 2, v7
	s_mov_b64 exec, s[20:21]
	ds_read_b32 v4, v4 offset:36640
	s_mov_b64 exec, s[22:23]
	ds_read_b32 v5, v5 offset:36640
	s_mov_b64 exec, s[24:25]
	ds_read_b32 v6, v6 offset:36640
	s_mov_b64 exec, s[26:27]
	ds_read_b32 v7, v7 offset:36640
	s_mov_b64 exec, -1
	s_waitcnt lgkmcnt(3)
	v_add_u32_e32 v4, v4, v60
	v_lshlrev_b32_e32 v4, 3, v4
	s_waitcnt lgkmcnt(2)
	v_add_u32_e32 v5, v5, v61
	v_lshlrev_b32_e32 v5, 3, v5
	s_waitcnt lgkmcnt(1)
	v_add_u32_e32 v6, v6, v62
	v_lshlrev_b32_e32 v6, 3, v6
	s_waitcnt lgkmcnt(0)
	v_add_u32_e32 v7, v7, v63
	v_lshlrev_b32_e32 v7, 3, v7
	s_mov_b64 exec, s[20:21]
	ds_write_b64 v4, v[28:29]
	s_mov_b64 exec, s[22:23]
	ds_write_b64 v5, v[30:31]
	s_mov_b64 exec, s[24:25]
	ds_write_b64 v6, v[32:33]
	s_mov_b64 exec, s[26:27]
	ds_write_b64 v7, v[34:35]
	s_mov_b64 exec, -1
	s_cmpk_lt_i32 s33, 0x401
	s_cbranch_scc1 .Lcsr_sc_done
	v_cmp_lt_i32_e64 s[20:21], -1, v36
	v_bfe_u32 v4, v36, 16, 7
	v_lshlrev_b32_e32 v4, 2, v4
	v_cmp_lt_i32_e64 s[22:23], -1, v38
	v_bfe_u32 v5, v38, 16, 7
	v_lshlrev_b32_e32 v5, 2, v5
	v_cmp_lt_i32_e64 s[24:25], -1, v40
	v_bfe_u32 v6, v40, 16, 7
	v_lshlrev_b32_e32 v6, 2, v6
	v_cmp_lt_i32_e64 s[26:27], -1, v42
	v_bfe_u32 v7, v42, 16, 7
	v_lshlrev_b32_e32 v7, 2, v7
	s_mov_b64 exec, s[20:21]
	ds_read_b32 v4, v4 offset:36640
	s_mov_b64 exec, s[22:23]
	ds_read_b32 v5, v5 offset:36640
	s_mov_b64 exec, s[24:25]
	ds_read_b32 v6, v6 offset:36640
	s_mov_b64 exec, s[26:27]
	ds_read_b32 v7, v7 offset:36640
	s_mov_b64 exec, -1
	s_waitcnt lgkmcnt(3)
	v_add_u32_e32 v4, v4, v64
	v_lshlrev_b32_e32 v4, 3, v4
	s_waitcnt lgkmcnt(2)
	v_add_u32_e32 v5, v5, v65
	v_lshlrev_b32_e32 v5, 3, v5
	s_waitcnt lgkmcnt(1)
	v_add_u32_e32 v6, v6, v66
	v_lshlrev_b32_e32 v6, 3, v6
	s_waitcnt lgkmcnt(0)
	v_add_u32_e32 v7, v7, v67
	v_lshlrev_b32_e32 v7, 3, v7
	s_mov_b64 exec, s[20:21]
	ds_write_b64 v4, v[36:37]
	s_mov_b64 exec, s[22:23]
	ds_write_b64 v5, v[38:39]
	s_mov_b64 exec, s[24:25]
	ds_write_b64 v6, v[40:41]
	s_mov_b64 exec, s[26:27]
	ds_write_b64 v7, v[42:43]
	s_mov_b64 exec, -1
	s_cmpk_lt_i32 s33, 0x801
	s_cbranch_scc1 .Lcsr_sc_done
	v_cmp_lt_i32_e64 s[20:21], -1, v44
	v_bfe_u32 v4, v44, 16, 7
	v_lshlrev_b32_e32 v4, 2, v4
	v_cmp_lt_i32_e64 s[22:23], -1, v46
	v_bfe_u32 v5, v46, 16, 7
	v_lshlrev_b32_e32 v5, 2, v5
	v_cmp_lt_i32_e64 s[24:25], -1, v48
	v_bfe_u32 v6, v48, 16, 7
	v_lshlrev_b32_e32 v6, 2, v6
	v_cmp_lt_i32_e64 s[26:27], -1, v50
	v_bfe_u32 v7, v50, 16, 7
	v_lshlrev_b32_e32 v7, 2, v7
	s_mov_b64 exec, s[20:21]
	ds_read_b32 v4, v4 offset:36640
	s_mov_b64 exec, s[22:23]
	ds_read_b32 v5, v5 offset:36640
	s_mov_b64 exec, s[24:25]
	ds_read_b32 v6, v6 offset:36640
	s_mov_b64 exec, s[26:27]
	ds_read_b32 v7, v7 offset:36640
	s_mov_b64 exec, -1
	s_waitcnt lgkmcnt(3)
	v_add_u32_e32 v4, v4, v68
	v_lshlrev_b32_e32 v4, 3, v4
	s_waitcnt lgkmcnt(2)
	v_add_u32_e32 v5, v5, v69
	v_lshlrev_b32_e32 v5, 3, v5
	s_waitcnt lgkmcnt(1)
	v_add_u32_e32 v6, v6, v70
	v_lshlrev_b32_e32 v6, 3, v6
	s_waitcnt lgkmcnt(0)
	v_add_u32_e32 v7, v7, v71
	v_lshlrev_b32_e32 v7, 3, v7
	s_mov_b64 exec, s[20:21]
	ds_write_b64 v4, v[44:45]
	s_mov_b64 exec, s[22:23]
	ds_write_b64 v5, v[46:47]
	s_mov_b64 exec, s[24:25]
	ds_write_b64 v6, v[48:49]
	s_mov_b64 exec, s[26:27]
	ds_write_b64 v7, v[50:51]
	s_mov_b64 exec, -1
	s_cmpk_lt_i32 s33, 0xc01
	s_cbranch_scc1 .Lcsr_sc_done
	v_cmp_lt_i32_e64 s[20:21], -1, v52
	v_bfe_u32 v4, v52, 16, 7
	v_lshlrev_b32_e32 v4, 2, v4
	v_cmp_lt_i32_e64 s[22:23], -1, v54
	v_bfe_u32 v5, v54, 16, 7
	v_lshlrev_b32_e32 v5, 2, v5
	v_cmp_lt_i32_e64 s[24:25], -1, v56
	v_bfe_u32 v6, v56, 16, 7
	v_lshlrev_b32_e32 v6, 2, v6
	v_cmp_lt_i32_e64 s[26:27], -1, v58
	v_bfe_u32 v7, v58, 16, 7
	v_lshlrev_b32_e32 v7, 2, v7
	s_mov_b64 exec, s[20:21]
	ds_read_b32 v4, v4 offset:36640
	s_mov_b64 exec, s[22:23]
	ds_read_b32 v5, v5 offset:36640
	s_mov_b64 exec, s[24:25]
	ds_read_b32 v6, v6 offset:36640
	s_mov_b64 exec, s[26:27]
	ds_read_b32 v7, v7 offset:36640
	s_mov_b64 exec, -1
	s_waitcnt lgkmcnt(3)
	v_add_u32_e32 v4, v4, v72
	v_lshlrev_b32_e32 v4, 3, v4
	s_waitcnt lgkmcnt(2)
	v_add_u32_e32 v5, v5, v73
	v_lshlrev_b32_e32 v5, 3, v5
	s_waitcnt lgkmcnt(1)
	v_add_u32_e32 v6, v6, v74
	v_lshlrev_b32_e32 v6, 3, v6
	s_waitcnt lgkmcnt(0)
	v_add_u32_e32 v7, v7, v75
	v_lshlrev_b32_e32 v7, 3, v7
	s_mov_b64 exec, s[20:21]
	ds_write_b64 v4, v[52:53]
	s_mov_b64 exec, s[22:23]
	ds_write_b64 v5, v[54:55]
	s_mov_b64 exec, s[24:25]
	ds_write_b64 v6, v[56:57]
	s_mov_b64 exec, s[26:27]
	ds_write_b64 v7, v[58:59]
	s_mov_b64 exec, -1
